# v8_vnop1_tail
# speedup vs baseline: 1.0022x; 1.0022x over previous
.Lchunk_loop:
	v_mfma_f32_16x16x32_f16 v[38:41], v[2:5], v[34:37], v[46:49]
	v_mfma_f32_16x16x32_f16 v[42:45], v[14:17], v[34:37], v[50:53]
	ds_read_b128 v[82:85], v94 offset:256
	ds_read_b128 v[86:89], v94 offset:272
	v_mfma_f32_16x16x32_f16 v[62:65], v[6:9], v[78:81], v[26:29]
	v_nop
	v_min_u32_e32 v1, v38, v40
	v_min_u32_e32 v0, v39, v41
	v_mfma_f32_16x16x32_f16 v[66:69], v[18:21], v[78:81], v[30:33]
	v_min3_u32 v1, v1, v42, v44
	v_min3_u32 v0, v0, v43, v45
	v_exp_f32_e32 v1, v1
	v_exp_f32_e32 v0, v0
	v_add_f32_e32 v1, 1.0, v1
	v_add_f32_e32 v0, 1.0, v0
	v_rcp_f32_e32 v1, v1
	v_rcp_f32_e32 v0, v0
	s_add_i32 s13, s8, 1
	v_cvt_pk_f16_f32 v34, v1, v0
	s_and_b32 s13, s13, 3
	s_mulk_i32 s13, 0x1100
	v_mov_b32_dpp v35, v34 quad_perm:[1,2,3,0] row_mask:0xf bank_mask:0xf bound_ctrl:1
	v_mov_b32_dpp v36, v34 quad_perm:[2,3,0,1] row_mask:0xf bank_mask:0xf bound_ctrl:1
	v_mov_b32_dpp v37, v34 quad_perm:[3,0,1,2] row_mask:0xf bank_mask:0xf bound_ctrl:1
	v_add_u32_e32 v95, s13, v177
	s_nop 0
	v_mfma_f32_16x16x32_f16 v[38:41], v[2:5], v[34:37], v[54:57]
	v_mfma_f32_16x16x32_f16 v[42:45], v[14:17], v[34:37], v[58:61]
	s_waitcnt lgkmcnt(0)
	v_mfma_f32_16x16x32_f16 v[70:73], v[10:13], v[78:81], v[26:29]
	v_nop
	v_min_u32_e32 v1, v38, v40
	v_min_u32_e32 v0, v39, v41
	v_mfma_f32_16x16x32_f16 v[74:77], v[22:25], v[78:81], v[30:33]
	v_min3_u32 v1, v1, v42, v44
	v_min3_u32 v0, v0, v43, v45
	v_exp_f32_e32 v1, v1
	v_exp_f32_e32 v0, v0
	v_add_f32_e32 v1, 1.0, v1
	v_add_f32_e32 v0, 1.0, v0
	v_rcp_f32_e32 v1, v1
	v_rcp_f32_e32 v0, v0
	v_cvt_pk_f16_f32 v78, v82, v83
	v_cvt_pk_f16_f32 v34, v1, v0
	v_cvt_pk_f16_f32 v79, v84, v85
	v_cvt_pk_f16_f32 v80, v86, v87
	v_mov_b32_dpp v35, v34 quad_perm:[1,2,3,0] row_mask:0xf bank_mask:0xf bound_ctrl:1
	v_mov_b32_dpp v36, v34 quad_perm:[2,3,0,1] row_mask:0xf bank_mask:0xf bound_ctrl:1
	v_mov_b32_dpp v37, v34 quad_perm:[3,0,1,2] row_mask:0xf bank_mask:0xf bound_ctrl:1
	v_cvt_pk_f16_f32 v81, v88, v89
	s_nop 0
	v_mfma_f32_16x16x32_f16 v[38:41], v[2:5], v[34:37], v[62:65]
	v_mfma_f32_16x16x32_f16 v[42:45], v[14:17], v[34:37], v[66:69]
	ds_read_b128 v[82:85], v94 offset:384
	ds_read_b128 v[86:89], v94 offset:400
	v_mfma_f32_16x16x32_f16 v[46:49], v[6:9], v[78:81], v[26:29]
	v_nop
	v_min_u32_e32 v1, v38, v40
	v_min_u32_e32 v0, v39, v41
	v_mfma_f32_16x16x32_f16 v[50:53], v[18:21], v[78:81], v[30:33]
	v_min3_u32 v1, v1, v42, v44
	v_min3_u32 v0, v0, v43, v45
	v_exp_f32_e32 v1, v1
	v_exp_f32_e32 v0, v0
	v_add_f32_e32 v1, 1.0, v1
	v_add_f32_e32 v0, 1.0, v0
	v_rcp_f32_e32 v1, v1
	v_rcp_f32_e32 v0, v0
	s_and_b32 s9, s8, 3
	v_cvt_pk_f16_f32 v34, v1, v0
	s_mulk_i32 s9, 0x1100
	s_add_i32 s9, s9, s24
	v_mov_b32_dpp v35, v34 quad_perm:[1,2,3,0] row_mask:0xf bank_mask:0xf bound_ctrl:1
	v_mov_b32_dpp v36, v34 quad_perm:[2,3,0,1] row_mask:0xf bank_mask:0xf bound_ctrl:1
	v_mov_b32_dpp v37, v34 quad_perm:[3,0,1,2] row_mask:0xf bank_mask:0xf bound_ctrl:1
	s_min_u32 s12, s8, 27
	s_lshl_b32 s22, s12, 10
	v_mfma_f32_16x16x32_f16 v[38:41], v[2:5], v[34:37], v[70:73]
	v_mfma_f32_16x16x32_f16 v[42:45], v[14:17], v[34:37], v[74:77]
	s_waitcnt lgkmcnt(0)
	v_mfma_f32_16x16x32_f16 v[54:57], v[10:13], v[78:81], v[26:29]
	v_nop
	v_min_u32_e32 v1, v38, v40
	v_min_u32_e32 v0, v39, v41
	v_mfma_f32_16x16x32_f16 v[58:61], v[22:25], v[78:81], v[30:33]
	v_min3_u32 v1, v1, v42, v44
	v_min3_u32 v0, v0, v43, v45
	v_exp_f32_e32 v1, v1
	v_exp_f32_e32 v0, v0
	v_add_f32_e32 v1, 1.0, v1
	v_add_f32_e32 v0, 1.0, v0
	v_rcp_f32_e32 v1, v1
	v_rcp_f32_e32 v0, v0
	v_cvt_pk_f16_f32 v78, v82, v83
	v_cvt_pk_f16_f32 v34, v1, v0
	v_cvt_pk_f16_f32 v79, v84, v85
	v_cvt_pk_f16_f32 v80, v86, v87
	v_mov_b32_dpp v35, v34 quad_perm:[1,2,3,0] row_mask:0xf bank_mask:0xf bound_ctrl:1
	v_mov_b32_dpp v36, v34 quad_perm:[2,3,0,1] row_mask:0xf bank_mask:0xf bound_ctrl:1
	v_mov_b32_dpp v37, v34 quad_perm:[3,0,1,2] row_mask:0xf bank_mask:0xf bound_ctrl:1
	v_cvt_pk_f16_f32 v81, v88, v89
	s_cmp_lt_u32 s8, 28
	s_cselect_b64 vcc, -1, 0
	v_mfma_f32_16x16x32_f16 v[38:41], v[2:5], v[34:37], v[46:49]
	v_mfma_f32_16x16x32_f16 v[42:45], v[14:17], v[34:37], v[50:53]
	ds_read_b128 v[82:85], v94 offset:512
	ds_read_b128 v[86:89], v94 offset:528
	v_mfma_f32_16x16x32_f16 v[62:65], v[6:9], v[78:81], v[26:29]
	v_nop
	v_min_u32_e32 v1, v38, v40
	v_min_u32_e32 v0, v39, v41
	v_mfma_f32_16x16x32_f16 v[66:69], v[18:21], v[78:81], v[30:33]
	v_min3_u32 v1, v1, v42, v44
	v_min3_u32 v0, v0, v43, v45
	v_exp_f32_e32 v1, v1
	v_exp_f32_e32 v0, v0
	v_add_f32_e32 v1, 1.0, v1
	v_add_f32_e32 v0, 1.0, v0
	v_rcp_f32_e32 v1, v1
	v_rcp_f32_e32 v0, v0
	v_lshl_add_u64 v[90:91], v[166:167], 0, s[22:23]
	v_cvt_pk_f16_f32 v34, v1, v0
	s_add_i32 s8, s8, 1
	s_nop 0
	v_mov_b32_dpp v35, v34 quad_perm:[1,2,3,0] row_mask:0xf bank_mask:0xf bound_ctrl:1
	v_mov_b32_dpp v36, v34 quad_perm:[2,3,0,1] row_mask:0xf bank_mask:0xf bound_ctrl:1
	v_mov_b32_dpp v37, v34 quad_perm:[3,0,1,2] row_mask:0xf bank_mask:0xf bound_ctrl:1
	s_nop 0
	s_nop 0
	v_mfma_f32_16x16x32_f16 v[38:41], v[2:5], v[34:37], v[54:57]
	v_mfma_f32_16x16x32_f16 v[42:45], v[14:17], v[34:37], v[58:61]
	s_waitcnt lgkmcnt(0)
	v_mfma_f32_16x16x32_f16 v[70:73], v[10:13], v[78:81], v[26:29]
	v_nop
	v_min_u32_e32 v1, v38, v40
	v_min_u32_e32 v0, v39, v41
	v_mfma_f32_16x16x32_f16 v[74:77], v[22:25], v[78:81], v[30:33]
	v_min3_u32 v1, v1, v42, v44
	v_min3_u32 v0, v0, v43, v45
	v_exp_f32_e32 v1, v1
	v_exp_f32_e32 v0, v0
	v_add_f32_e32 v1, 1.0, v1
	v_add_f32_e32 v0, 1.0, v0
	v_rcp_f32_e32 v1, v1
	v_rcp_f32_e32 v0, v0
	v_cvt_pk_f16_f32 v78, v82, v83
	v_cvt_pk_f16_f32 v34, v1, v0
	v_cvt_pk_f16_f32 v79, v84, v85
	v_cvt_pk_f16_f32 v80, v86, v87
	v_mov_b32_dpp v35, v34 quad_perm:[1,2,3,0] row_mask:0xf bank_mask:0xf bound_ctrl:1
	v_mov_b32_dpp v36, v34 quad_perm:[2,3,0,1] row_mask:0xf bank_mask:0xf bound_ctrl:1
	v_mov_b32_dpp v37, v34 quad_perm:[3,0,1,2] row_mask:0xf bank_mask:0xf bound_ctrl:1
	v_cvt_pk_f16_f32 v81, v88, v89
	s_nop 0
	v_mfma_f32_16x16x32_f16 v[38:41], v[2:5], v[34:37], v[62:65]
	v_mfma_f32_16x16x32_f16 v[42:45], v[14:17], v[34:37], v[66:69]
	ds_read_b128 v[82:85], v94 offset:640
	ds_read_b128 v[86:89], v94 offset:656
	v_mfma_f32_16x16x32_f16 v[46:49], v[6:9], v[78:81], v[26:29]
	v_nop
	v_min_u32_e32 v1, v38, v40
	v_min_u32_e32 v0, v39, v41
	v_mfma_f32_16x16x32_f16 v[50:53], v[18:21], v[78:81], v[30:33]
	v_min3_u32 v1, v1, v42, v44
	v_min3_u32 v0, v0, v43, v45
	v_exp_f32_e32 v1, v1
	v_exp_f32_e32 v0, v0
	v_add_f32_e32 v1, 1.0, v1
	v_add_f32_e32 v0, 1.0, v0
	v_rcp_f32_e32 v1, v1
	v_rcp_f32_e32 v0, v0
	v_lshl_add_u64 v[92:93], v[90:91], 0, s[0:1]
	v_cvt_pk_f16_f32 v34, v1, v0
	v_lshl_add_u64 v[96:97], v[90:91], 0, s[2:3]
	v_lshl_add_u64 v[98:99], v[90:91], 0, s[4:5]
	v_mov_b32_dpp v35, v34 quad_perm:[1,2,3,0] row_mask:0xf bank_mask:0xf bound_ctrl:1
	v_mov_b32_dpp v36, v34 quad_perm:[2,3,0,1] row_mask:0xf bank_mask:0xf bound_ctrl:1
	v_mov_b32_dpp v37, v34 quad_perm:[3,0,1,2] row_mask:0xf bank_mask:0xf bound_ctrl:1
	v_lshl_add_u64 v[100:101], v[90:91], 0, s[6:7]
	s_nop 0
	v_mfma_f32_16x16x32_f16 v[38:41], v[2:5], v[34:37], v[70:73]
	v_mfma_f32_16x16x32_f16 v[42:45], v[14:17], v[34:37], v[74:77]
	s_waitcnt lgkmcnt(0)
	v_mfma_f32_16x16x32_f16 v[54:57], v[10:13], v[78:81], v[26:29]
	v_nop
	v_min_u32_e32 v1, v38, v40
	v_min_u32_e32 v0, v39, v41
	v_mfma_f32_16x16x32_f16 v[58:61], v[22:25], v[78:81], v[30:33]
	v_min3_u32 v1, v1, v42, v44
	v_min3_u32 v0, v0, v43, v45
	v_exp_f32_e32 v1, v1
	v_exp_f32_e32 v0, v0
	v_add_f32_e32 v1, 1.0, v1
	v_add_f32_e32 v0, 1.0, v0
	v_rcp_f32_e32 v1, v1
	v_rcp_f32_e32 v0, v0
	v_cvt_pk_f16_f32 v78, v82, v83
	v_cvt_pk_f16_f32 v34, v1, v0
	v_cvt_pk_f16_f32 v79, v84, v85
	v_cvt_pk_f16_f32 v80, v86, v87
	v_mov_b32_dpp v35, v34 quad_perm:[1,2,3,0] row_mask:0xf bank_mask:0xf bound_ctrl:1
	v_mov_b32_dpp v36, v34 quad_perm:[2,3,0,1] row_mask:0xf bank_mask:0xf bound_ctrl:1
	v_mov_b32_dpp v37, v34 quad_perm:[3,0,1,2] row_mask:0xf bank_mask:0xf bound_ctrl:1
	v_cvt_pk_f16_f32 v81, v88, v89
	s_nop 0
	v_mfma_f32_16x16x32_f16 v[38:41], v[2:5], v[34:37], v[46:49]
	v_mfma_f32_16x16x32_f16 v[42:45], v[14:17], v[34:37], v[50:53]
	ds_read_b128 v[82:85], v94 offset:768
	ds_read_b128 v[86:89], v94 offset:784
	v_mfma_f32_16x16x32_f16 v[62:65], v[6:9], v[78:81], v[26:29]
	v_nop
	v_min_u32_e32 v1, v38, v40
	v_min_u32_e32 v0, v39, v41
	v_mfma_f32_16x16x32_f16 v[66:69], v[18:21], v[78:81], v[30:33]
	v_min3_u32 v1, v1, v42, v44
	v_min3_u32 v0, v0, v43, v45
	v_exp_f32_e32 v1, v1
	v_exp_f32_e32 v0, v0
	v_add_f32_e32 v1, 1.0, v1
	v_add_f32_e32 v0, 1.0, v0
	v_rcp_f32_e32 v1, v1
	v_rcp_f32_e32 v0, v0
	s_nop 0
	v_cvt_pk_f16_f32 v34, v1, v0
	s_nop 0
	s_nop 0
	v_mov_b32_dpp v35, v34 quad_perm:[1,2,3,0] row_mask:0xf bank_mask:0xf bound_ctrl:1
	v_mov_b32_dpp v36, v34 quad_perm:[2,3,0,1] row_mask:0xf bank_mask:0xf bound_ctrl:1
	v_mov_b32_dpp v37, v34 quad_perm:[3,0,1,2] row_mask:0xf bank_mask:0xf bound_ctrl:1
	s_nop 0
	s_nop 0
	v_mfma_f32_16x16x32_f16 v[38:41], v[2:5], v[34:37], v[54:57]
	v_mfma_f32_16x16x32_f16 v[42:45], v[14:17], v[34:37], v[58:61]
	s_waitcnt lgkmcnt(0)
	v_mfma_f32_16x16x32_f16 v[70:73], v[10:13], v[78:81], v[26:29]
	v_nop
	v_min_u32_e32 v1, v38, v40
	v_min_u32_e32 v0, v39, v41
	v_mfma_f32_16x16x32_f16 v[74:77], v[22:25], v[78:81], v[30:33]
	v_min3_u32 v1, v1, v42, v44
	v_min3_u32 v0, v0, v43, v45
	v_exp_f32_e32 v1, v1
	v_exp_f32_e32 v0, v0
	v_add_f32_e32 v1, 1.0, v1
	v_add_f32_e32 v0, 1.0, v0
	v_rcp_f32_e32 v1, v1
	v_rcp_f32_e32 v0, v0
	v_cvt_pk_f16_f32 v78, v82, v83
	v_cvt_pk_f16_f32 v34, v1, v0
	v_cvt_pk_f16_f32 v79, v84, v85
	v_cvt_pk_f16_f32 v80, v86, v87
	v_mov_b32_dpp v35, v34 quad_perm:[1,2,3,0] row_mask:0xf bank_mask:0xf bound_ctrl:1
	v_mov_b32_dpp v36, v34 quad_perm:[2,3,0,1] row_mask:0xf bank_mask:0xf bound_ctrl:1
	v_mov_b32_dpp v37, v34 quad_perm:[3,0,1,2] row_mask:0xf bank_mask:0xf bound_ctrl:1
	v_cvt_pk_f16_f32 v81, v88, v89
	s_nop 0
	v_mfma_f32_16x16x32_f16 v[38:41], v[2:5], v[34:37], v[62:65]
	v_mfma_f32_16x16x32_f16 v[42:45], v[14:17], v[34:37], v[66:69]
	ds_read_b128 v[82:85], v94 offset:896
	ds_read_b128 v[86:89], v94 offset:912
	v_mfma_f32_16x16x32_f16 v[46:49], v[6:9], v[78:81], v[26:29]
	v_nop
	v_min_u32_e32 v1, v38, v40
	v_min_u32_e32 v0, v39, v41
	v_mfma_f32_16x16x32_f16 v[50:53], v[18:21], v[78:81], v[30:33]
	v_min3_u32 v1, v1, v42, v44
	v_min3_u32 v0, v0, v43, v45
	v_exp_f32_e32 v1, v1
	v_exp_f32_e32 v0, v0
	v_add_f32_e32 v1, 1.0, v1
	v_add_f32_e32 v0, 1.0, v0
	v_rcp_f32_e32 v1, v1
	v_rcp_f32_e32 v0, v0
	s_nop 0
	v_cvt_pk_f16_f32 v34, v1, v0
	s_nop 0
	s_nop 0
	v_mov_b32_dpp v35, v34 quad_perm:[1,2,3,0] row_mask:0xf bank_mask:0xf bound_ctrl:1
	v_mov_b32_dpp v36, v34 quad_perm:[2,3,0,1] row_mask:0xf bank_mask:0xf bound_ctrl:1
	v_mov_b32_dpp v37, v34 quad_perm:[3,0,1,2] row_mask:0xf bank_mask:0xf bound_ctrl:1
	s_nop 0
	s_nop 0
	v_mfma_f32_16x16x32_f16 v[38:41], v[2:5], v[34:37], v[70:73]
	s_waitcnt vmcnt(8)
	s_cbranch_vccz .Ltail_wait
.Ltail_back:
	s_mov_b32 m0, s9
	v_mfma_f32_16x16x32_f16 v[42:45], v[14:17], v[34:37], v[74:77]
	s_waitcnt lgkmcnt(0)
	v_mfma_f32_16x16x32_f16 v[54:57], v[10:13], v[78:81], v[26:29]
	v_nop
	v_min_u32_e32 v1, v38, v40
	v_min_u32_e32 v0, v39, v41
	v_mfma_f32_16x16x32_f16 v[58:61], v[22:25], v[78:81], v[30:33]
	v_min3_u32 v1, v1, v42, v44
	v_min3_u32 v0, v0, v43, v45
	v_exp_f32_e32 v1, v1
	v_exp_f32_e32 v0, v0
	v_add_f32_e32 v1, 1.0, v1
	v_add_f32_e32 v0, 1.0, v0
	v_rcp_f32_e32 v1, v1
	v_rcp_f32_e32 v0, v0
	v_cvt_pk_f16_f32 v78, v82, v83
	v_cvt_pk_f16_f32 v34, v1, v0
	v_cvt_pk_f16_f32 v79, v84, v85
	v_cvt_pk_f16_f32 v80, v86, v87
	v_mov_b32_dpp v35, v34 quad_perm:[1,2,3,0] row_mask:0xf bank_mask:0xf bound_ctrl:1
	v_mov_b32_dpp v36, v34 quad_perm:[2,3,0,1] row_mask:0xf bank_mask:0xf bound_ctrl:1
	v_mov_b32_dpp v37, v34 quad_perm:[3,0,1,2] row_mask:0xf bank_mask:0xf bound_ctrl:1
	v_cvt_pk_f16_f32 v81, v88, v89
	s_nop 0
	v_mfma_f32_16x16x32_f16 v[38:41], v[2:5], v[34:37], v[46:49]
	s_cbranch_vccz .Lskip_dma12
	global_load_lds_dwordx4 v[92:93], off nt
.Lskip_dma12:
	s_add_i32 m0, s9, 0x440
	v_mfma_f32_16x16x32_f16 v[42:45], v[14:17], v[34:37], v[50:53]
	ds_read_b128 v[82:85], v95
	ds_read_b128 v[86:89], v95 offset:16
	v_mfma_f32_16x16x32_f16 v[62:65], v[6:9], v[78:81], v[26:29]
	v_nop
	v_min_u32_e32 v1, v38, v40
	v_min_u32_e32 v0, v39, v41
	v_mfma_f32_16x16x32_f16 v[66:69], v[18:21], v[78:81], v[30:33]
	v_min3_u32 v1, v1, v42, v44
	v_min3_u32 v0, v0, v43, v45
	v_exp_f32_e32 v1, v1
	v_exp_f32_e32 v0, v0
	v_add_f32_e32 v1, 1.0, v1
	v_add_f32_e32 v0, 1.0, v0
	v_rcp_f32_e32 v1, v1
	v_rcp_f32_e32 v0, v0
	s_nop 0
	v_cvt_pk_f16_f32 v34, v1, v0
	s_nop 0
	s_nop 0
	v_mov_b32_dpp v35, v34 quad_perm:[1,2,3,0] row_mask:0xf bank_mask:0xf bound_ctrl:1
	v_mov_b32_dpp v36, v34 quad_perm:[2,3,0,1] row_mask:0xf bank_mask:0xf bound_ctrl:1
	v_mov_b32_dpp v37, v34 quad_perm:[3,0,1,2] row_mask:0xf bank_mask:0xf bound_ctrl:1
	s_nop 0
	s_nop 0
	v_mfma_f32_16x16x32_f16 v[38:41], v[2:5], v[34:37], v[54:57]
	s_cbranch_vccz .Lskip_dma13
	global_load_lds_dwordx4 v[96:97], off nt
.Lskip_dma13:
	s_add_i32 m0, s9, 0x880
	v_mfma_f32_16x16x32_f16 v[42:45], v[14:17], v[34:37], v[58:61]
	s_waitcnt lgkmcnt(0)
	v_mfma_f32_16x16x32_f16 v[70:73], v[10:13], v[78:81], v[26:29]
	v_nop
	v_min_u32_e32 v1, v38, v40
	v_min_u32_e32 v0, v39, v41
	v_mfma_f32_16x16x32_f16 v[74:77], v[22:25], v[78:81], v[30:33]
	v_min3_u32 v1, v1, v42, v44
	v_min3_u32 v0, v0, v43, v45
	v_exp_f32_e32 v1, v1
	v_exp_f32_e32 v0, v0
	v_add_f32_e32 v1, 1.0, v1
	v_add_f32_e32 v0, 1.0, v0
	v_rcp_f32_e32 v1, v1
	v_rcp_f32_e32 v0, v0
	v_cvt_pk_f16_f32 v78, v82, v83
	v_cvt_pk_f16_f32 v34, v1, v0
	v_cvt_pk_f16_f32 v79, v84, v85
	v_cvt_pk_f16_f32 v80, v86, v87
	v_mov_b32_dpp v35, v34 quad_perm:[1,2,3,0] row_mask:0xf bank_mask:0xf bound_ctrl:1
	v_mov_b32_dpp v36, v34 quad_perm:[2,3,0,1] row_mask:0xf bank_mask:0xf bound_ctrl:1
	v_mov_b32_dpp v37, v34 quad_perm:[3,0,1,2] row_mask:0xf bank_mask:0xf bound_ctrl:1
	v_cvt_pk_f16_f32 v81, v88, v89
	s_nop 0
	v_mfma_f32_16x16x32_f16 v[38:41], v[2:5], v[34:37], v[62:65]
	s_cbranch_vccz .Lskip_dma14
	global_load_lds_dwordx4 v[98:99], off nt
.Lskip_dma14:
	s_add_i32 m0, s9, 0xcc0
	v_mfma_f32_16x16x32_f16 v[42:45], v[14:17], v[34:37], v[66:69]
	ds_read_b128 v[82:85], v95 offset:128
	ds_read_b128 v[86:89], v95 offset:144
	v_mfma_f32_16x16x32_f16 v[46:49], v[6:9], v[78:81], v[26:29]
	v_nop
	v_min_u32_e32 v1, v38, v40
	v_min_u32_e32 v0, v39, v41
	v_mfma_f32_16x16x32_f16 v[50:53], v[18:21], v[78:81], v[30:33]
	v_min3_u32 v1, v1, v42, v44
	v_min3_u32 v0, v0, v43, v45
	v_exp_f32_e32 v1, v1
	v_exp_f32_e32 v0, v0
	v_add_f32_e32 v1, 1.0, v1
	v_add_f32_e32 v0, 1.0, v0
	v_rcp_f32_e32 v1, v1
	v_rcp_f32_e32 v0, v0
	v_mov_b32_e32 v94, v95
	v_cvt_pk_f16_f32 v34, v1, v0
	s_nop 0
	s_nop 0
	v_mov_b32_dpp v35, v34 quad_perm:[1,2,3,0] row_mask:0xf bank_mask:0xf bound_ctrl:1
	v_mov_b32_dpp v36, v34 quad_perm:[2,3,0,1] row_mask:0xf bank_mask:0xf bound_ctrl:1
	v_mov_b32_dpp v37, v34 quad_perm:[3,0,1,2] row_mask:0xf bank_mask:0xf bound_ctrl:1
	s_nop 0
	s_nop 0
	v_mfma_f32_16x16x32_f16 v[38:41], v[2:5], v[34:37], v[70:73]
	s_cbranch_vccz .Lskip_dma15
	global_load_lds_dwordx4 v[100:101], off nt
.Lskip_dma15:
	v_mfma_f32_16x16x32_f16 v[42:45], v[14:17], v[34:37], v[74:77]
	s_waitcnt lgkmcnt(0)
	v_mfma_f32_16x16x32_f16 v[54:57], v[10:13], v[78:81], v[26:29]
	v_nop
	v_min_u32_e32 v1, v38, v40
	v_min_u32_e32 v0, v39, v41
	v_mfma_f32_16x16x32_f16 v[58:61], v[22:25], v[78:81], v[30:33]
	v_min3_u32 v1, v1, v42, v44
	v_min3_u32 v0, v0, v43, v45
	v_exp_f32_e32 v1, v1
	v_exp_f32_e32 v0, v0
	v_add_f32_e32 v1, 1.0, v1
	v_add_f32_e32 v0, 1.0, v0
	v_rcp_f32_e32 v1, v1
	v_rcp_f32_e32 v0, v0
	v_cvt_pk_f16_f32 v78, v82, v83
	v_cvt_pk_f16_f32 v34, v1, v0
	v_cvt_pk_f16_f32 v79, v84, v85
	v_cvt_pk_f16_f32 v80, v86, v87
	v_mov_b32_dpp v35, v34 quad_perm:[1,2,3,0] row_mask:0xf bank_mask:0xf bound_ctrl:1
	v_mov_b32_dpp v36, v34 quad_perm:[2,3,0,1] row_mask:0xf bank_mask:0xf bound_ctrl:1
	v_mov_b32_dpp v37, v34 quad_perm:[3,0,1,2] row_mask:0xf bank_mask:0xf bound_ctrl:1
	v_cvt_pk_f16_f32 v81, v88, v89
	s_nop 0
	s_cmp_eq_u32 s8, 32
	s_cbranch_scc0 .Lchunk_loop
	s_branch .Lepilogue
